# Fourier stage B: input tiles prefetched two units ahead into alternating register sets (was one unit ahead), top-of-unit wait counts loads and stores still in flight; plus previous changes
# baseline (speedup 1.0000x reference)
; #define FB_LOAD(u) do { const int _b = (u) >> 9, _k1 = ((u) >> 2) & 127, _cb = (u) & 3; \
;         _Pragma("unroll") for (int _q = 0; _q < 4; ++_q) pf[_q] = *(const bf16x8*)(F.zm() + (size_t)((_b * 128 + _k1) * 64 + (_q & 1) * 32 + sr) * DM + (_q >> 1) * 512 + _cb * 128 + sc); } while (0)
; __device__ __forceinline__ void phase_fft_b(const Frame& F) {
;     ...
;     const int NU = NB * 128 * 4;
;     bf16x8 pf[4];
;     ...
;     int u = F.wg, par = 0;
;     if (u < NU) FB_LOAD(u);
.LBB0_508:
	s_andn2_b64 vcc, exec, s[8:9]
	s_cbranch_vccnz .LBB0_585
	v_readlane_b32 s8, v252, 42
	s_waitcnt vmcnt(0)
	v_mov_b32_e32 v2, v0
	v_readlane_b32 s9, v252, 43
	s_andn2_b64 vcc, exec, s[8:9]
	v_readfirstlane_b32 s0, v2
	v_mov_b32_e32 v136, 0xffff8000
	v_mov_b32_e32 v137, 0xffffa000
	v_mov_b32_e32 v138, 0xffffc000
	v_mov_b32_e32 v139, 0xa000
	v_mov_b32_e32 v140, 0xc000
	v_mov_b32_e32 v141, 0x10000
	v_mov_b32_e32 v142, 0x12000
	v_mov_b32_e32 v143, 0x14000
	v_mov_b32_e32 v144, 0x16000
	v_mov_b32_e32 v145, 0x18000
	v_mov_b32_e32 v148, 0x1a000
	v_mov_b32_e32 v149, 0x1c000
	s_cbranch_vccnz .LBB0_516
	s_lshr_b32 s1, s0, 1
	s_add_u32 s8, s56, 0xd0000
	v_and_b32_e32 v1, 31, v2
	s_addc_u32 s9, s57, 0
	v_and_or_b32 v1, s1, 32, v1
	s_add_u32 s18, s56, 0xd2000
	v_bfe_u32 v3, v2, 5, 1
	s_addc_u32 s19, s57, 0
	v_lshlrev_b32_e32 v1, 7, v1
	s_add_u32 s22, s56, 0xd4000
	v_lshl_or_b32 v4, v3, 4, v1
	v_ashrrev_i32_e32 v100, 4, v2
	v_readlane_b32 s1, v253, 1
	s_addc_u32 s23, s57, 0
	v_or_b32_e32 v5, 32, v4
	v_add_u32_e32 v6, s1, v100
	global_load_dwordx4 v[34:37], v4, s[8:9]
	global_load_dwordx4 v[38:41], v4, s[18:19]
	global_load_dwordx4 v[42:45], v4, s[22:23]
	global_load_dwordx4 v[46:49], v5, s[8:9]
	global_load_dwordx4 v[50:53], v5, s[18:19]
	global_load_dwordx4 v[54:57], v5, s[22:23]
	v_or_b32_e32 v5, 64, v4
	s_ashr_i32 s0, s0, 7
	v_ashrrev_i32_e32 v7, 31, v6
	global_load_dwordx4 v[58:61], v5, s[8:9]
	global_load_dwordx4 v[62:65], v5, s[18:19]
	v_or_b32_e32 v4, 0x60, v4
	global_load_dwordx4 v[66:69], v5, s[22:23]
	global_load_dwordx4 v[70:73], v4, s[8:9]
	global_load_dwordx4 v[74:77], v4, s[18:19]
	global_load_dwordx4 v[78:81], v4, s[22:23]
	s_add_u32 s8, s56, 0x3d316100
	v_lshlrev_b64 v[8:9], 11, v[6:7]
	v_add_u32_e32 v6, 32, v6
	v_lshlrev_b32_e32 v5, 3, v2
	s_addc_u32 s9, s57, 0
	v_readlane_b32 s1, v252, 57
	v_ashrrev_i32_e32 v7, 31, v6
	v_and_b32_e32 v4, 0x78, v5
	v_lshl_add_u64 v[8:9], s[8:9], 0, v[8:9]
	s_lshl_b32 s76, s1, 1
	v_lshlrev_b64 v[6:7], 11, v[6:7]
	v_lshl_add_u64 v[8:9], v[8:9], 0, s[76:77]
	v_lshlrev_b32_e32 v146, 1, v4
	v_lshl_add_u64 v[6:7], s[8:9], 0, v[6:7]
	v_lshl_add_u64 v[8:9], v[8:9], 0, v[146:147]
	v_lshl_add_u64 v[6:7], v[6:7], 0, s[76:77]
	v_lshl_add_u64 v[6:7], v[6:7], 0, v[146:147]
	global_load_dwordx4 v[82:85], v[8:9], off
	global_load_dwordx4 v[86:89], v[8:9], off offset:1024
	global_load_dwordx4 v[90:93], v[6:7], off
	global_load_dwordx4 v[94:97], v[6:7], off offset:1024
	v_lshrrev_b32_e32 v7, 1, v100
	v_and_b32_e32 v8, 3, v100
	v_and_b32_e32 v6, 63, v2
	v_and_or_b32 v7, v7, 4, v8
	v_lshlrev_b32_e32 v101, 6, v7
	v_lshlrev_b32_e32 v7, 4, v2
	v_lshlrev_b32_e32 v6, 3, v6
	v_and_b32_e32 v102, 48, v7
	v_and_b32_e32 v8, 24, v6
	v_and_b32_e32 v7, 0xc0, v7
	v_lshlrev_b32_e32 v2, 1, v2
	s_lshl_b32 s1, s0, 9
	v_and_b32_e32 v2, 32, v2
	v_and_b32_e32 v6, 0x100, v6
	v_or3_b32 v7, v7, s1, v8
	v_or3_b32 v103, v7, v2, v6
	v_lshlrev_b32_e32 v2, 2, v3
	v_and_b32_e32 v3, 0xfffff0, v100
	v_lshlrev_b32_e32 v6, 1, v100
	v_and_or_b32 v3, v6, 8, v3
	v_bfe_u32 v5, v5, 5, 2
	v_lshrrev_b32_e32 v3, 1, v3
	v_or_b32_e32 v3, v3, v5
	v_lshlrev_b32_e32 v104, 9, v3
	v_add_u32_e32 v3, 32, v100
	v_and_b32_e32 v6, 0xfffff0, v3
	v_lshlrev_b32_e32 v3, 1, v3
	s_lshl_b32 s18, s0, 5
	v_and_or_b32 v3, v3, 8, v6
	s_ashr_i32 s19, s18, 31
	v_lshrrev_b32_e32 v3, 1, v3
	v_or_b32_e32 v3, v3, v5
	s_add_u32 s22, s56, 0x1c316100
	v_readlane_b32 s24, v254, 62
	v_lshlrev_b32_e32 v105, 9, v3
	s_addc_u32 s23, s57, 0
	s_mov_b32 s0, 0
	v_lshlrev_b32_e32 v98, 1, v4
	v_lshlrev_b32_e32 v146, 1, v2
	v_readlane_b32 s1, v254, 6
	v_readlane_b32 s30, v253, 15
	s_mov_b32 s31, s24
	v_readlane_b32 s25, v254, 63
	v_and_b32_e32 v122, 31, v0
	v_mul_u32_u24_e32 v122, 0x90, v122
	v_bfe_u32 v123, v0, 5, 1
	v_lshl_add_u32 v122, v123, 3, v122
	v_lshrrev_b32_e32 v123, 6, v0
	v_mul_u32_u24_e32 v123, 0x1200, v123
	v_add_u32_e32 v123, 0x12800, v123
	v_add_u32_e32 v122, v122, v123
	v_bfe_u32 v124, v0, 2, 4
	v_mul_u32_u24_e32 v124, 0x90, v124
	v_add_u32_e32 v123, v123, v124
	v_and_b32_e32 v124, 3, v0
	v_lshl_add_u32 v123, v124, 4, v123
	v_bfe_u32 v1, v0, 2, 4
	v_bfe_u32 v124, v0, 6, 1
	v_lshl_or_b32 v1, v124, 5, v1
	v_lshlrev_b32_e32 v1, 7, v1
	v_and_b32_e32 v146, 3, v0
	v_lshlrev_b32_e32 v146, 4, v146
	s_add_i32 s100, s31, s96
	s_cmpk_gt_i32 s100, 0xfff
	s_cbranch_scc1 .Lfb_pro_nopf
	s_lshl_b32 s101, s100, 4
	s_andn2_b32 s101, s101, 63
	v_add_u32_e32 v2, s101, v100
	s_lshl_b32 s101, s100, 7
	v_ashrrev_i32_e32 v3, 31, v2
	s_and_b32 s28, s101, 0x180
	v_lshlrev_b64 v[4:5], 11, v[2:3]
	v_add_u32_e32 v2, 32, v2
	v_ashrrev_i32_e32 v3, 31, v2
	v_lshl_add_u64 v[4:5], s[8:9], 0, v[4:5]
	s_lshl_b32 s76, s28, 1
	v_lshlrev_b64 v[2:3], 11, v[2:3]
	v_lshl_add_u64 v[4:5], v[4:5], 0, s[76:77]
	v_mov_b32_e32 v99, v147
	v_lshl_add_u64 v[2:3], s[8:9], 0, v[2:3]
	v_lshl_add_u64 v[4:5], v[4:5], 0, v[98:99]
	v_lshl_add_u64 v[2:3], v[2:3], 0, s[76:77]
	v_lshl_add_u64 v[2:3], v[2:3], 0, v[98:99]
	global_load_dwordx4 v[198:201], v[4:5], off
	global_load_dwordx4 v[202:205], v[4:5], off offset:1024
	global_load_dwordx4 v[206:209], v[2:3], off
	global_load_dwordx4 v[210:213], v[2:3], off offset:1024
	s_add_i32 s100, s100, s96
	s_waitcnt vmcnt(4)
	s_branch .LBB0_512
.Lfb_pro_nopf:
	s_waitcnt vmcnt(0)
	s_branch .LBB0_512

; #define LAS __attribute__((address_space(3)))
; __device__ __forceinline__ int v_st(int k, int c) { const int kk = (k & ~0xC) | ((k & 4) << 1) | ((k & 8) >> 1); return ((kk >> 3) * 4 + (c >> 5)) * 512 + ((kk & 7) * 32 + (c & 31)) * 2; }
; __device__ __forceinline__ void phase_fft_b(const Frame& F) {
;     ...
;     for (; u < NU; u += F.nwg, par ^= 1) {
;         const int b = u >> 9, k1 = (u >> 2) & 127, cb = u & 3;
;         LAS char* img = Vt + par * 32768;
; #pragma unroll
;         for (int q = 0; q < 4; ++q) *(LAS bf16x8*)(img + (q >> 1) * 16384 + ff::v_st((q & 1) * 32 + sr, sc)) = pf[q];
;         __syncthreads();
.LBB0_512:
	s_lshl_b32 s2, s0, 15
	s_add_i32 s40, s2, 0
	s_add_i32 s2, s31, s96
	v_add_u32_e32 v2, s40, v104
	v_add_u32_e32 v3, s40, v105
	v_add3_u32 v2, v2, v101, v102
	v_add3_u32 v3, v3, v101, v102
	v_readlane_b32 s7, v254, 4
	s_add_i32 s7, s30, s7
	s_cmpk_gt_i32 s2, 0xfff
	s_cselect_b64 s[24:25], -1, 0
	s_cbranch_scc1 .Lfb_w0
	s_waitcnt vmcnt(8)
	s_branch .Lfb_w1

; #define LAS __attribute__((address_space(3)))
; __device__ __forceinline__ int v_st(int k, int c) { const int kk = (k & ~0xC) | ((k & 4) << 1) | ((k & 8) >> 1); return ((kk >> 3) * 4 + (c >> 5)) * 512 + ((kk & 7) * 32 + (c & 31)) * 2; }
; #define FB_LOAD(u) do { const int _b = (u) >> 9, _k1 = ((u) >> 2) & 127, _cb = (u) & 3; \
;         _Pragma("unroll") for (int _q = 0; _q < 4; ++_q) pf[_q] = *(const bf16x8*)(F.zm() + (size_t)((_b * 128 + _k1) * 64 + (_q & 1) * 32 + sr) * DM + (_q >> 1) * 512 + _cb * 128 + sc); } while (0)
; __device__ __forceinline__ void phase_fft_b(const Frame& F) {
;     ...
;         LAS char* img = Vt + par * 32768;
; #pragma unroll
;         for (int q = 0; q < 4; ++q) *(LAS bf16x8*)(img + (q >> 1) * 16384 + ff::v_st((q & 1) * 32 + sr, sc)) = pf[q];
;         __syncthreads();
;         if (u + F.nwg < NU) FB_LOAD(u + F.nwg);
.Lfb_w1:
	s_cmp_lg_u32 s0, 0
	s_cbranch_scc1 .Lfb_top_b
	ds_write_b128 v2, v[82:85]
	ds_write_b128 v3, v[90:93]
	ds_write_b128 v2, v[86:89] offset:16384
	ds_write_b128 v3, v[94:97] offset:16384
	s_waitcnt lgkmcnt(0)
	s_barrier
	s_cmpk_gt_i32 s100, 0xfff
	s_cbranch_scc1 .LBB0_511
	s_lshl_b32 s101, s100, 4
	s_andn2_b32 s101, s101, 63
	v_add_u32_e32 v2, s101, v100
	s_lshl_b32 s101, s100, 7
	v_ashrrev_i32_e32 v3, 31, v2
	s_and_b32 s28, s101, 0x180
	v_lshlrev_b64 v[4:5], 11, v[2:3]
	v_add_u32_e32 v2, 32, v2
	v_ashrrev_i32_e32 v3, 31, v2
	v_lshl_add_u64 v[4:5], s[8:9], 0, v[4:5]
	s_lshl_b32 s76, s28, 1
	v_lshlrev_b64 v[2:3], 11, v[2:3]
	v_lshl_add_u64 v[4:5], v[4:5], 0, s[76:77]
	v_mov_b32_e32 v99, v147
	v_lshl_add_u64 v[2:3], s[8:9], 0, v[2:3]
	v_lshl_add_u64 v[4:5], v[4:5], 0, v[98:99]
	v_lshl_add_u64 v[2:3], v[2:3], 0, s[76:77]
	v_lshl_add_u64 v[2:3], v[2:3], 0, v[98:99]
	global_load_dwordx4 v[82:85], v[4:5], off
	global_load_dwordx4 v[86:89], v[4:5], off offset:1024
	global_load_dwordx4 v[90:93], v[2:3], off
	global_load_dwordx4 v[94:97], v[2:3], off offset:1024
	s_add_i32 s100, s100, s96
	s_branch .LBB0_511
.Lfb_top_b:
	ds_write_b128 v2, v[198:201]
	ds_write_b128 v3, v[206:209]
	ds_write_b128 v2, v[202:205] offset:16384
	ds_write_b128 v3, v[210:213] offset:16384
	s_waitcnt lgkmcnt(0)
	s_barrier
	s_cmpk_gt_i32 s100, 0xfff
	s_cbranch_scc1 .LBB0_511
	s_lshl_b32 s101, s100, 4
	s_andn2_b32 s101, s101, 63
	v_add_u32_e32 v2, s101, v100
	s_lshl_b32 s101, s100, 7
	v_ashrrev_i32_e32 v3, 31, v2
	s_and_b32 s28, s101, 0x180
	v_lshlrev_b64 v[4:5], 11, v[2:3]
	v_add_u32_e32 v2, 32, v2
	v_ashrrev_i32_e32 v3, 31, v2
	v_lshl_add_u64 v[4:5], s[8:9], 0, v[4:5]
	s_lshl_b32 s76, s28, 1
	v_lshlrev_b64 v[2:3], 11, v[2:3]
	v_lshl_add_u64 v[4:5], v[4:5], 0, s[76:77]
	v_mov_b32_e32 v99, v147
	v_lshl_add_u64 v[2:3], s[8:9], 0, v[2:3]
	v_lshl_add_u64 v[4:5], v[4:5], 0, v[98:99]
	v_lshl_add_u64 v[2:3], v[2:3], 0, s[76:77]
	v_lshl_add_u64 v[2:3], v[2:3], 0, v[98:99]
	global_load_dwordx4 v[198:201], v[4:5], off
	global_load_dwordx4 v[202:205], v[4:5], off offset:1024
	global_load_dwordx4 v[206:209], v[2:3], off
	global_load_dwordx4 v[210:213], v[2:3], off offset:1024
	s_add_i32 s100, s100, s96
	s_branch .LBB0_511
